# adds: P12 unit loop header vmcnt(0) drain removed (previous unit's epilogue store acks overlap the next unit's setup; the K-loop's counted waits cover older ops)
# speedup vs baseline: 1.0013x; 1.0013x over previous
.LBB0_1502:
	ds_read_b32 v2, v226
	s_add_i32 s2, s2, 1
	v_readlane_b32 s18, v254, 33
	s_mul_i32 s18, s2, s18
	s_add_i32 s21, s59, s18
	s_waitcnt lgkmcnt(0)
	v_readfirstlane_b32 s18, v2
	s_min_i32 s23, s18, s60
	s_cmp_gt_i32 s23, s21
	s_cselect_b64 s[18:19], -1, 0
	s_cmp_le_i32 s23, s21
	s_cbranch_scc1 .LBB0_1504
	v_lshlrev_b32_e32 v2, 2, v194
	v_add_u32_e32 v2, 0x20100, v2
	ds_read_b32 v2, v2
	s_waitcnt lgkmcnt(0)
	v_cmp_ge_i32_e32 vcc, s21, v2
	s_and_b32 vcc_lo, vcc_lo, -2
	s_bcnt1_i32_b32 s12, vcc_lo
	s_lshl_b32 s3, s12, 2
	s_add_i32 s3, s3, 0
	s_add_i32 s3, s3, 0x20100
	v_mov_b32_e32 v4, s3
	ds_read2st64_b32 v[2:3], v4 offset1:1
	s_waitcnt lgkmcnt(0)
	v_readfirstlane_b32 s3, v2
	ds_read_b32 v2, v4 offset:512
	s_sub_i32 s3, s21, s3
	s_abs_i32 s35, s3
	v_readfirstlane_b32 s23, v3
	s_waitcnt lgkmcnt(0)
	v_readfirstlane_b32 s44, v2
	s_add_i32 s21, s44, 0xff
	s_ashr_i32 s21, s21, 8
	s_abs_i32 s38, s21
	v_cvt_f32_u32_e32 v2, s38
	s_sub_i32 s39, 0, s38
	s_xor_b32 s34, s3, s21
	s_ashr_i32 s34, s34, 31
	v_rcp_iflag_f32_e32 v2, v2
	s_nop 0
	v_mul_f32_e32 v2, 0x4f7ffffe, v2
	v_cvt_u32_f32_e32 v2, v2
	s_nop 0
	v_readfirstlane_b32 s40, v2
	s_mul_i32 s39, s39, s40
	s_mul_hi_u32 s39, s40, s39
	s_add_i32 s40, s40, s39
	s_mul_hi_u32 s39, s35, s40
	s_mul_i32 s40, s39, s38
	s_sub_i32 s35, s35, s40
	s_add_i32 s40, s39, 1
	s_sub_i32 s41, s35, s38
	s_cmp_ge_u32 s35, s38
	s_cselect_b32 s39, s40, s39
	s_cselect_b32 s35, s41, s35
	s_add_i32 s40, s39, 1
	s_cmp_ge_u32 s35, s38
	s_cselect_b32 s35, s40, s39
	s_xor_b32 s35, s35, s34
	s_sub_i32 s42, s35, s34
	s_mul_i32 s21, s21, s42
	s_sub_i32 s3, s3, s21
	s_lshl_b32 s21, s3, 8
	s_add_i32 s34, s21, s23
	s_ashr_i32 s35, s34, 31
	s_lshl_b64 s[38:39], s[34:35], 11
	v_readlane_b32 s3, v254, 38
	s_add_u32 s38, s3, s38
	v_readlane_b32 s3, v254, 40
	s_addc_u32 s39, s3, s39
	s_lshl_b64 s[40:41], s[12:13], 22
	s_add_u32 s3, s52, s40
	s_addc_u32 s23, s53, s41
	s_ashr_i32 s43, s42, 31
	s_lshl_b64 s[40:41], s[42:43], 19
	s_add_u32 s40, s3, s40
	s_addc_u32 s41, s23, s41
	s_sub_i32 s21, s44, s21
	s_lshl_b32 s3, s42, 8
	s_min_i32 s35, s21, 0x100
